# diff tile loop: s_waitcnt vmcnt(0) for the next tile's K/V loads placed before the PV MFMAs (loads retire mid-tile) on top of v044
# speedup vs baseline: 1.0128x; 1.0012x over previous
.LBB0_1022:
	v_exp_f32_e32 v82, v82
	v_exp_f32_e32 v83, v83
	v_exp_f32_e32 v84, v84
	v_exp_f32_e32 v85, v85
	v_exp_f32_e32 v86, v86
	v_exp_f32_e32 v87, v87
	v_exp_f32_e32 v88, v88
	v_exp_f32_e32 v89, v89
	v_exp_f32_e32 v90, v90
	v_exp_f32_e32 v91, v91
	v_exp_f32_e32 v92, v92
	v_exp_f32_e32 v93, v93
	v_exp_f32_e32 v94, v94
	v_exp_f32_e32 v95, v95
	v_exp_f32_e32 v96, v96
	v_exp_f32_e32 v97, v97
	v_exp_f32_e32 v98, v98
	v_exp_f32_e32 v99, v99
	v_exp_f32_e32 v100, v100
	v_exp_f32_e32 v101, v101
	v_exp_f32_e32 v102, v102
	v_exp_f32_e32 v103, v103
	v_exp_f32_e32 v104, v104
	v_exp_f32_e32 v105, v105
	v_exp_f32_e32 v106, v106
	v_exp_f32_e32 v107, v107
	v_exp_f32_e32 v108, v108
	v_exp_f32_e32 v109, v109
	v_exp_f32_e32 v110, v110
	v_exp_f32_e32 v111, v111
	v_exp_f32_e32 v112, v112
	v_exp_f32_e32 v113, v113
	v_pk_add_f32 v[146:147], v[82:83], v[98:99]
	v_pk_add_f32 v[148:149], v[84:85], v[100:101]
	v_pk_add_f32 v[146:147], v[146:147], v[86:87]
	v_pk_add_f32 v[148:149], v[148:149], v[102:103]
	v_pk_add_f32 v[146:147], v[146:147], v[88:89]
	v_pk_add_f32 v[148:149], v[148:149], v[104:105]
	v_pk_add_f32 v[146:147], v[146:147], v[90:91]
	v_pk_add_f32 v[148:149], v[148:149], v[106:107]
	v_pk_add_f32 v[146:147], v[146:147], v[92:93]
	v_pk_add_f32 v[148:149], v[148:149], v[108:109]
	v_pk_add_f32 v[146:147], v[146:147], v[94:95]
	v_pk_add_f32 v[148:149], v[148:149], v[110:111]
	v_pk_add_f32 v[146:147], v[146:147], v[96:97]
	v_pk_add_f32 v[148:149], v[148:149], v[112:113]
	v_pk_add_f32 v[146:147], v[146:147], v[148:149]
	v_cvt_pk_bf16_f32 v82, v82, v83
	v_cvt_pk_bf16_f32 v83, v84, v85
	v_cvt_pk_bf16_f32 v84, v86, v87
	v_cvt_pk_bf16_f32 v85, v88, v89
	v_cvt_pk_bf16_f32 v90, v90, v91
	v_cvt_pk_bf16_f32 v91, v92, v93
	v_cvt_pk_bf16_f32 v92, v94, v95
	v_cvt_pk_bf16_f32 v93, v96, v97
	v_add_f32_e32 v146, v146, v147
	v_cvt_pk_bf16_f32 v86, v98, v99
	v_cvt_pk_bf16_f32 v87, v100, v101
	v_cvt_pk_bf16_f32 v88, v102, v103
	v_cvt_pk_bf16_f32 v89, v104, v105
	v_cvt_pk_bf16_f32 v94, v106, v107
	v_cvt_pk_bf16_f32 v95, v108, v109
	v_cvt_pk_bf16_f32 v96, v110, v111
	v_cvt_pk_bf16_f32 v97, v112, v113
	v_add3_u32 v148, s22, v240, v241
	v_add_f32_e32 v205, v205, v146
	ds_read_b64_tr_b16 v[98:99], v148 offset:17536
	ds_read_b64_tr_b16 v[100:101], v148 offset:20096
	ds_read_b64_tr_b16 v[102:103], v148 offset:22656
	ds_read_b64_tr_b16 v[104:105], v148 offset:25216
	ds_read_b64_tr_b16 v[106:107], v148 offset:27776
	ds_read_b64_tr_b16 v[108:109], v148 offset:30336
	ds_read_b64_tr_b16 v[110:111], v148 offset:32896
	ds_read_b64_tr_b16 v[112:113], v148 offset:35456
	s_waitcnt lgkmcnt(8)
	s_waitcnt vmcnt(0)
	v_mfma_f32_32x32x16_bf16 v[50:65], v[150:153], v[82:85], v[50:65]
	v_mfma_f32_32x32x16_bf16 v[50:65], v[154:157], v[90:93], v[50:65]
	v_mfma_f32_32x32x16_bf16 v[50:65], v[158:161], v[86:89], v[50:65]
	v_mfma_f32_32x32x16_bf16 v[50:65], v[162:165], v[94:97], v[50:65]
	ds_read_b64_tr_b16 v[150:151], v148 offset:17600
	ds_read_b64_tr_b16 v[152:153], v148 offset:20160
	ds_read_b64_tr_b16 v[154:155], v148 offset:22720
	ds_read_b64_tr_b16 v[156:157], v148 offset:25280
	ds_read_b64_tr_b16 v[158:159], v148 offset:27840
	ds_read_b64_tr_b16 v[160:161], v148 offset:30400
	ds_read_b64_tr_b16 v[162:163], v148 offset:32960
	ds_read_b64_tr_b16 v[164:165], v148 offset:35520
	v_mfma_f32_32x32x16_bf16 v[34:49], v[166:169], v[82:85], v[34:49]
	v_mfma_f32_32x32x16_bf16 v[34:49], v[170:173], v[90:93], v[34:49]
	v_mfma_f32_32x32x16_bf16 v[34:49], v[174:177], v[86:89], v[34:49]
	v_mfma_f32_32x32x16_bf16 v[34:49], v[216:219], v[94:97], v[34:49]
	s_waitcnt lgkmcnt(8)
	v_mfma_f32_32x32x16_bf16 v[18:33], v[98:101], v[82:85], v[18:33]
	v_mfma_f32_32x32x16_bf16 v[18:33], v[102:105], v[90:93], v[18:33]
	v_mfma_f32_32x32x16_bf16 v[18:33], v[106:109], v[86:89], v[18:33]
	v_mfma_f32_32x32x16_bf16 v[18:33], v[110:113], v[94:97], v[18:33]
	s_waitcnt lgkmcnt(0)
	v_mfma_f32_32x32x16_bf16 v[2:17], v[150:153], v[82:85], v[2:17]
	v_mfma_f32_32x32x16_bf16 v[2:17], v[154:157], v[90:93], v[2:17]
	v_mfma_f32_32x32x16_bf16 v[2:17], v[158:161], v[86:89], v[2:17]
	v_mfma_f32_32x32x16_bf16 v[2:17], v[162:165], v[94:97], v[2:17]
	s_andn2_b64 vcc, exec, s[6:7]
	s_cbranch_vccnz .LBB0_1007
